# baseline (speedup 1.0000x reference)
.LBB2_14:
	v_cvt_pk_bf16_f32 v156, v198, v199
	v_cvt_pk_bf16_f32 v157, v230, v231
	v_cvt_pk_bf16_f32 v158, v232, v233
	v_cvt_pk_bf16_f32 v159, v234, v235
	v_cvt_pk_bf16_f32 v160, v148, v149
	v_cvt_pk_bf16_f32 v161, v150, v151
	v_cvt_pk_bf16_f32 v162, v152, v153
	v_cvt_pk_bf16_f32 v163, v154, v155
	v_exp_f32_e32 v128, v112
	v_exp_f32_e32 v129, v113
	v_mfma_f32_32x32x16_bf16 a[48:63], v[60:63], v[140:143], a[48:63]
	v_exp_f32_e32 v130, v114
	v_exp_f32_e32 v131, v115
	v_mfma_f32_32x32x16_bf16 a[64:79], v[56:59], v[52:55], a[64:79]
	v_add_f32_e32 v60, v201, v128
	v_add_f32_e32 v61, v201, v129
	v_exp_f32_e32 v132, v116
	v_exp_f32_e32 v133, v117
	v_exp_f32_e32 v134, v118
	v_mfma_f32_32x32x16_bf16 a[80:95], v[56:59], v[140:143], a[80:95]
	v_add_f32_e32 v56, v60, v130
	v_add_f32_e32 v57, v61, v131
	v_exp_f32_e32 v135, v119
	v_exp_f32_e32 v136, v120
	v_mfma_f32_32x32x16_bf16 a[96:111], v[48:51], v[52:55], a[96:111]
	v_add_f32_e32 v52, v56, v132
	v_add_f32_e32 v53, v57, v133
	v_add_f32_e32 v52, v52, v134
	v_exp_f32_e32 v137, v121
	v_exp_f32_e32 v138, v122
	v_exp_f32_e32 v139, v123
	v_mfma_f32_32x32x16_bf16 a[112:127], v[48:51], v[140:143], a[112:127]
	v_add_f32_e32 v48, v53, v135
	v_add_f32_e32 v49, v52, v136
	v_exp_f32_e32 v140, v124
	v_exp_f32_e32 v141, v125
	v_mfma_f32_32x32x16_bf16 a[0:15], v[44:47], v[156:159], a[0:15]
	v_add_f32_e32 v48, v48, v137
	v_add_f32_e32 v49, v49, v138
	v_add_f32_e32 v48, v48, v139
	v_exp_f32_e32 v142, v126
	v_exp_f32_e32 v143, v127
	v_exp_f32_e32 v144, v96
	v_mfma_f32_32x32x16_bf16 a[16:31], v[44:47], v[160:163], a[16:31]
	v_add_f32_e32 v44, v49, v140
	v_add_f32_e32 v45, v48, v141
	v_exp_f32_e32 v145, v97
	v_exp_f32_e32 v146, v98
	v_mfma_f32_32x32x16_bf16 a[32:47], v[40:43], v[156:159], a[32:47]
	v_add_f32_e32 v237, v44, v142
	v_add_f32_e32 v236, v45, v143
	v_add_f32_e32 v44, v201, v144
	v_exp_f32_e32 v147, v99
	v_exp_f32_e32 v148, v100
	v_exp_f32_e32 v149, v101
	v_mfma_f32_32x32x16_bf16 a[48:63], v[40:43], v[160:163], a[48:63]
	v_add_f32_e32 v40, v201, v145
	v_add_f32_e32 v41, v44, v146
	v_exp_f32_e32 v150, v102
	v_exp_f32_e32 v151, v103
	v_mfma_f32_32x32x16_bf16 a[64:79], v[36:39], v[156:159], a[64:79]
	v_add_f32_e32 v40, v40, v147
	v_add_f32_e32 v41, v41, v148
	v_add_f32_e32 v40, v40, v149
	v_exp_f32_e32 v152, v104
	v_exp_f32_e32 v153, v105
	v_exp_f32_e32 v154, v106
	v_mfma_f32_32x32x16_bf16 a[80:95], v[36:39], v[160:163], a[80:95]
	v_add_f32_e32 v36, v41, v150
	v_add_f32_e32 v37, v40, v151
	v_mfma_f32_32x32x16_bf16 a[96:111], v[32:35], v[156:159], a[96:111]
	v_exp_f32_e32 v155, v107
	v_exp_f32_e32 v156, v108
	v_add_f32_e32 v36, v36, v152
	v_add_f32_e32 v37, v37, v153
	v_add_f32_e32 v36, v36, v154
	v_exp_f32_e32 v157, v109
	v_exp_f32_e32 v158, v110
	v_exp_f32_e32 v159, v111
	v_mfma_f32_32x32x16_bf16 a[112:127], v[32:35], v[160:163], a[112:127]
	v_add_f32_e32 v32, v37, v155
	v_add_f32_e32 v33, v36, v156
	s_andn2_b64 vcc, exec, s[0:1]
	v_add_f32_e32 v32, v32, v157
	v_add_f32_e32 v238, v33, v158
	v_add_f32_e32 v239, v32, v159
	s_cbranch_vccz .LBB2_19

.LBB2_16:
	v_cvt_pk_bf16_f32 v156, v198, v199
	v_cvt_pk_bf16_f32 v157, v230, v231
	v_cvt_pk_bf16_f32 v158, v232, v233
	v_cvt_pk_bf16_f32 v159, v234, v235
	v_cvt_pk_bf16_f32 v160, v148, v149
	v_cvt_pk_bf16_f32 v161, v150, v151
	v_cvt_pk_bf16_f32 v162, v152, v153
	v_cvt_pk_bf16_f32 v163, v154, v155
	v_exp_f32_e32 v128, v112
	v_exp_f32_e32 v129, v113
	v_mfma_f32_32x32x16_bf16 a[48:63], v[92:95], v[140:143], a[48:63]
	v_exp_f32_e32 v130, v114
	v_exp_f32_e32 v131, v115
	v_mfma_f32_32x32x16_bf16 a[64:79], v[88:91], v[84:87], a[64:79]
	v_add_f32_e32 v92, v201, v128
	v_add_f32_e32 v93, v201, v129
	v_exp_f32_e32 v132, v116
	v_exp_f32_e32 v133, v117
	v_exp_f32_e32 v134, v118
	v_mfma_f32_32x32x16_bf16 a[80:95], v[88:91], v[140:143], a[80:95]
	v_add_f32_e32 v88, v92, v130
	v_add_f32_e32 v89, v93, v131
	v_exp_f32_e32 v135, v119
	v_exp_f32_e32 v136, v120
	v_mfma_f32_32x32x16_bf16 a[96:111], v[80:83], v[84:87], a[96:111]
	v_add_f32_e32 v84, v88, v132
	v_add_f32_e32 v85, v89, v133
	v_add_f32_e32 v84, v84, v134
	v_exp_f32_e32 v137, v121
	v_exp_f32_e32 v138, v122
	v_exp_f32_e32 v139, v123
	v_mfma_f32_32x32x16_bf16 a[112:127], v[80:83], v[140:143], a[112:127]
	v_add_f32_e32 v80, v85, v135
	v_add_f32_e32 v81, v84, v136
	v_exp_f32_e32 v140, v124
	v_exp_f32_e32 v141, v125
	v_mfma_f32_32x32x16_bf16 a[0:15], v[76:79], v[156:159], a[0:15]
	v_add_f32_e32 v80, v80, v137
	v_add_f32_e32 v81, v81, v138
	v_add_f32_e32 v80, v80, v139
	v_exp_f32_e32 v142, v126
	v_exp_f32_e32 v143, v127
	v_exp_f32_e32 v144, v96
	v_mfma_f32_32x32x16_bf16 a[16:31], v[76:79], v[160:163], a[16:31]
	v_add_f32_e32 v76, v81, v140
	v_add_f32_e32 v77, v80, v141
	v_exp_f32_e32 v145, v97
	v_exp_f32_e32 v146, v98
	v_mfma_f32_32x32x16_bf16 a[32:47], v[72:75], v[156:159], a[32:47]
	v_add_f32_e32 v239, v76, v142
	v_add_f32_e32 v238, v77, v143
	v_add_f32_e32 v76, v201, v144
	v_exp_f32_e32 v147, v99
	v_exp_f32_e32 v148, v100
	v_exp_f32_e32 v149, v101
	v_mfma_f32_32x32x16_bf16 a[48:63], v[72:75], v[160:163], a[48:63]
	v_add_f32_e32 v72, v201, v145
	v_add_f32_e32 v73, v76, v146
	v_exp_f32_e32 v150, v102
	v_exp_f32_e32 v151, v103
	v_mfma_f32_32x32x16_bf16 a[64:79], v[68:71], v[156:159], a[64:79]
	v_add_f32_e32 v72, v72, v147
	v_add_f32_e32 v73, v73, v148
	v_add_f32_e32 v72, v72, v149
	v_exp_f32_e32 v152, v104
	v_exp_f32_e32 v153, v105
	v_exp_f32_e32 v154, v106
	v_mfma_f32_32x32x16_bf16 a[80:95], v[68:71], v[160:163], a[80:95]
	v_add_f32_e32 v68, v73, v150
	v_add_f32_e32 v69, v72, v151
	v_mfma_f32_32x32x16_bf16 a[96:111], v[64:67], v[156:159], a[96:111]
	v_exp_f32_e32 v155, v107
	v_exp_f32_e32 v156, v108
	v_add_f32_e32 v68, v68, v152
	v_add_f32_e32 v69, v69, v153
	v_add_f32_e32 v68, v68, v154
	v_exp_f32_e32 v157, v109
	v_exp_f32_e32 v158, v110
	v_exp_f32_e32 v159, v111
	v_mfma_f32_32x32x16_bf16 a[112:127], v[64:67], v[160:163], a[112:127]
	v_add_f32_e32 v64, v69, v155
	v_add_f32_e32 v65, v68, v156
	s_andn2_b64 vcc, exec, s[0:1]
	v_add_f32_e32 v64, v64, v157
	v_add_f32_e32 v240, v65, v158
	v_add_f32_e32 v241, v64, v159
	s_cbranch_vccz .LBB2_21
